# DeltaNet scan: the two compute waves no longer issue LDS-DMA, waves 2-3 issue their pieces as well (after the split barrier)
# baseline (speedup 1.0000x reference)
.Lscan_w23:
	s_barrier
	s_add_u32 s10, s59, s13
	s_addc_u32 s11, s60, 0
	s_sub_u32 s10, s10, 0x4800
	s_subb_u32 s11, s11, 0
	s_add_i32 m0, s15, s17
	s_sub_i32 m0, m0, 0x4800
	v_lshl_add_u64 v[66:67], s[10:11], 0, v[130:131]
	global_load_lds_dwordx4 v[66:67], off nt
	s_add_u32 s10, s61, s13
	s_addc_u32 s11, s62, 0
	s_sub_u32 s10, s10, 0x4800
	s_subb_u32 s11, s11, 0
	s_add_i32 m0, s15, s19
	s_sub_i32 m0, m0, 0x4800
	v_lshl_add_u64 v[66:67], s[10:11], 0, v[130:131]
	global_load_lds_dwordx4 v[66:67], off nt
	s_add_u32 s10, s63, s69
	s_addc_u32 s11, s64, 0
	s_sub_u32 s10, s10, 0x4800
	s_subb_u32 s11, s11, 0
	s_add_i32 m0, s15, s21
	s_sub_i32 m0, m0, 0x4800
	v_lshl_add_u64 v[66:67], s[10:11], 0, v[130:131]
	global_load_lds_dwordx4 v[66:67], off nt
	s_add_u32 s10, s65, s69
	s_addc_u32 s11, s66, 0
	s_sub_u32 s10, s10, 0x4800
	s_subb_u32 s11, s11, 0
	s_add_i32 m0, s15, s23
	s_sub_i32 m0, m0, 0x4800
	v_lshl_add_u64 v[66:67], s[10:11], 0, v[130:131]
	global_load_lds_dwordx4 v[66:67], off nt
	s_add_u32 s10, s67, s69
	s_addc_u32 s11, s86, 0
	s_sub_u32 s10, s10, 0x4800
	s_subb_u32 s11, s11, 0
	s_add_i32 m0, s15, s25
	s_sub_i32 m0, m0, 0x4800
	v_lshl_add_u64 v[66:67], s[10:11], 0, v[130:131]
	global_load_lds_dwordx4 v[66:67], off nt
	s_add_u32 s10, s87, s69
	s_addc_u32 s11, s94, 0
	s_sub_u32 s10, s10, 0x4800
	s_subb_u32 s11, s11, 0
	s_add_i32 m0, s15, s27
	s_sub_i32 m0, m0, 0x4800
	v_lshl_add_u64 v[66:67], s[10:11], 0, v[130:131]
	global_load_lds_dwordx4 v[66:67], off nt
	s_add_u32 s10, s95, s69
	s_addc_u32 s11, s96, 0
	s_sub_u32 s10, s10, 0x4800
	s_subb_u32 s11, s11, 0
	s_add_i32 m0, s15, s29
	s_sub_i32 m0, m0, 0x4800
	v_lshl_add_u64 v[66:67], s[10:11], 0, v[130:131]
	global_load_lds_dwordx4 v[66:67], off nt
	s_add_u32 s10, s97, s69
	s_addc_u32 s11, s42, 0
	s_sub_u32 s10, s10, 0x4800
	s_subb_u32 s11, s11, 0
	s_add_i32 m0, s15, s31
	s_sub_i32 m0, m0, 0x4800
	v_lshl_add_u64 v[66:67], s[10:11], 0, v[130:131]
	global_load_lds_dwordx4 v[66:67], off nt
	s_add_u32 s10, s43, s69
	s_addc_u32 s11, s52, 0
	s_sub_u32 s10, s10, 0x4800
	s_subb_u32 s11, s11, 0
	s_add_i32 m0, s15, s48
	s_sub_i32 m0, m0, 0x4800
	v_lshl_add_u64 v[66:67], s[10:11], 0, v[130:131]
	global_load_lds_dwordx4 v[66:67], off nt
	s_branch .LBB0_715

.LBB0_728:
	s_lshl_b32 s8, s10, 3
	s_add_i32 s12, s8, s45
	s_ashr_i32 s13, s12, 31
	s_lshl_b64 s[8:9], s[12:13], 15
	s_mul_i32 s14, s12, 0xe000
	s_bitcmp1_b32 s70, 0
	s_cselect_b32 s15, 0x12000, 0
	s_cmp_lg_u64 s[0:1], 0
	s_cselect_b32 s13, s8, s14
	s_cmp_lg_u64 s[4:5], 0
	s_cselect_b32 s69, s14, s8
	s_and_b64 vcc, exec, s[6:7]
	s_cbranch_vccnz .LBB0_765
	s_add_u32 s10, s59, s13
	s_addc_u32 s11, s60, 0
	s_add_i32 m0, s15, s17
	v_lshl_add_u64 v[66:67], s[10:11], 0, v[130:131]
	global_load_lds_dwordx4 v[66:67], off nt
	s_add_u32 s10, s61, s13
	s_addc_u32 s11, s62, 0
	s_add_i32 m0, s15, s19
	v_lshl_add_u64 v[66:67], s[10:11], 0, v[130:131]
	global_load_lds_dwordx4 v[66:67], off nt
	s_add_u32 s10, s63, s69
	s_addc_u32 s11, s64, 0
	s_add_i32 m0, s15, s21
	v_lshl_add_u64 v[66:67], s[10:11], 0, v[130:131]
	global_load_lds_dwordx4 v[66:67], off nt
	s_add_u32 s10, s65, s69
	s_addc_u32 s11, s66, 0
	s_add_i32 m0, s15, s23
	v_lshl_add_u64 v[66:67], s[10:11], 0, v[130:131]
	global_load_lds_dwordx4 v[66:67], off nt
	s_add_u32 s10, s67, s69
	s_addc_u32 s11, s86, 0
	s_add_i32 m0, s15, s25
	v_lshl_add_u64 v[66:67], s[10:11], 0, v[130:131]
	global_load_lds_dwordx4 v[66:67], off nt
	s_add_u32 s10, s87, s69
	s_addc_u32 s11, s94, 0
	s_add_i32 m0, s15, s27
	v_lshl_add_u64 v[66:67], s[10:11], 0, v[130:131]
	global_load_lds_dwordx4 v[66:67], off nt
	s_add_u32 s10, s95, s69
	s_addc_u32 s11, s96, 0
	s_add_i32 m0, s15, s29
	v_lshl_add_u64 v[66:67], s[10:11], 0, v[130:131]
	global_load_lds_dwordx4 v[66:67], off nt
	s_add_u32 s10, s97, s69
	s_addc_u32 s11, s42, 0
	s_add_i32 m0, s15, s31
	v_lshl_add_u64 v[66:67], s[10:11], 0, v[130:131]
	global_load_lds_dwordx4 v[66:67], off nt
	s_add_u32 s10, s43, s69
	s_addc_u32 s11, s52, 0
	s_add_i32 m0, s15, s48
	v_lshl_add_u64 v[66:67], s[10:11], 0, v[130:131]
	global_load_lds_dwordx4 v[66:67], off nt
	s_andn2_b64 vcc, exec, s[6:7]
	s_cbranch_vccnz .Lscan_w2
